# MoE up/down GEMM units dealt by the XCD-aware virtual workgroup index (8 column tiles of a row block on one XCD); s_nop padding around the lane writes
# baseline (speedup 1.0000x reference)
; #define LAS __attribute__((address_space(3)))
; #define SEAM(k) do { if (IN(k) && IN((k) + 1)) GRID_BAR(); } while (0)
; template <unsigned PHMASK> __global__ void __launch_bounds__(NTHR, 2) fwd(Args args) {
;     extern __shared__ __attribute__((aligned(16))) unsigned char lds_raw[];
;     Frame F;
;     F.lds = (LAS unsigned char*)lds_raw; F.ws = args.ws; F.ctl = (gu32*)(args.ws + WS_CTL);
;     F.tid = threadIdx.x; F.lane = F.tid & 63; F.wave = __builtin_amdgcn_readfirstlane(F.tid >> 6); F.G = gridDim.x; F.bx = blockIdx.x;
;     const int wave0 = F.wave;
;     volatile LAS unsigned* MISC = (volatile LAS unsigned*)(F.lds + MISC_OFF);
;     if (F.tid < 64) MISC[F.tid] = 0u;
;     if (F.tid == 0) { LAS unsigned long long* P = (LAS unsigned long long*)(F.lds + PTR_OFF);
; #pragma unroll
;         for (int i = 0; i < 26; ++i) P[i] = (unsigned long long)args.in[i];
;         P[26] = (unsigned long long)args.out; P[27] = (unsigned long long)args.ws; }
;     __syncthreads();
;     ...
;     XcdBarrier bar = xcd_barrier_post((unsigned*)(F.ctl + CW_BAR), MISC + 8);
;     ...
;     const int lo = args.ph_lo, hi = args.ph_hi;
;     ...
;     if (PHON(0) && IN(0)) for (int dup_ = 0; dup_ < (DUP_PHASE == 0 ? 2 : 1); ++dup_) { PHASE_FENCE(); p0_prologue(args, F); __syncthreads(); } SEAM(0);
;     for (int l = 0; l < DEPTH; ++l) {
;         const int pb = 1 + l * PH_PER_LAYER;
.LBB0_202:
	s_cmpk_lt_i32 s92, 0xdc0
	s_cselect_b64 s[16:17], -1, 0
	s_ashr_i32 s93, s92, 31
	s_lshr_b32 s0, s93, 29
	s_add_i32 s0, s92, s0
	s_ashr_i32 s7, s0, 3
	s_ashr_i32 s53, s52, 31
	s_add_u32 s4, s2, 0x4200
	s_addc_u32 s5, s3, 0
	v_writelane_b32 v249, s4, 7
	s_mov_b32 s18, 2.0
	s_mov_b32 s74, 0x41000000
	v_writelane_b32 v249, s5, 8
	s_add_u32 s4, s2, 0x4400
	s_addc_u32 s5, s3, 0
	v_writelane_b32 v249, s4, 9
	s_mov_b32 s36, 0x41200000
	s_mov_b32 s26, 0x41800000
	v_writelane_b32 v249, s5, 10
	s_add_u32 s4, s2, 0x4500
	s_addc_u32 s5, s3, 0
	v_writelane_b32 v249, s4, 11
	s_mov_b32 s56, 0x41900000
	s_mov_b32 s22, 0x41c00000
	v_writelane_b32 v249, s5, 12
	s_add_u32 s4, s2, 0x4600
	s_addc_u32 s5, s3, 0
	v_writelane_b32 v249, s4, 13
	s_mov_b32 s24, 0x41d00000
	s_mov_b32 s30, 0x42680000
	v_writelane_b32 v249, s5, 14
	s_add_u32 s4, s2, 0x4700
	s_addc_u32 s5, s3, 0
	v_writelane_b32 v249, s4, 15
	s_mov_b32 s20, 0x42600000
	s_mov_b32 s34, 0x42480000
	v_writelane_b32 v249, s5, 16
	s_add_u32 s4, s2, 0x4800
	s_addc_u32 s5, s3, 0
	v_writelane_b32 v249, s4, 17
	s_mov_b32 s80, 0x42400000
	s_mov_b32 s76, 0x42280000
	v_writelane_b32 v249, s5, 18
	s_add_u32 s4, s2, 0x4900
	s_addc_u32 s5, s3, 0
	v_writelane_b32 v249, s4, 19
	s_mov_b32 s82, 0x42200000
	s_mov_b32 s84, 0x42080000
	v_writelane_b32 v249, s5, 20
	s_add_u32 s4, s2, 0x4a00
	s_addc_u32 s5, s3, 0
	v_writelane_b32 v249, s4, 21
	s_mov_b32 s86, 0x42000000
	s_mov_b32 s89, 0
	v_writelane_b32 v249, s5, 22
	s_add_u32 s4, s2, 0x4b00
	s_addc_u32 s5, s3, 0
	v_writelane_b32 v249, s4, 23
	v_mov_b32_e32 v1, 0
	v_mov_b32_e32 v223, 1
	v_writelane_b32 v249, s5, 24
	s_add_u32 s4, s2, 0x4c00
	s_addc_u32 s5, s3, 0
	v_writelane_b32 v249, s4, 25
	v_mov_b32_e32 v224, 1.0
	v_mov_b32_e32 v225, 0x3ecc95a3
	v_writelane_b32 v249, s5, 26
	s_add_u32 s4, s2, 0x4d00
	s_addc_u32 s5, s3, 0
	v_writelane_b32 v249, s4, 27
	v_mov_b32_e32 v226, 0x3c088889
	v_mov_b32_e32 v227, 0x260
	v_writelane_b32 v249, s5, 28
	s_add_u32 s4, s2, 0x4e00
	s_addc_u32 s5, s3, 0
	v_writelane_b32 v249, s4, 29
	s_mov_b32 s19, 0x40400000
	s_mov_b32 s75, 0x41100000
	v_writelane_b32 v249, s5, 30
	s_add_u32 s4, s2, 0x4f00
	s_addc_u32 s5, s3, 0
	v_writelane_b32 v249, s4, 31
	s_mov_b32 s37, 0x41300000
	s_mov_b32 s27, 0x41880000
	v_writelane_b32 v249, s5, 32
	s_add_u32 s4, s2, 0x5000
	s_addc_u32 s5, s3, 0
	v_writelane_b32 v249, s4, 33
	s_mov_b32 s57, 0x41980000
	s_mov_b32 s23, 0x41c80000
	v_writelane_b32 v249, s5, 34
	s_add_u32 s4, s2, 0x5100
	s_addc_u32 s5, s3, 0
	v_writelane_b32 v249, s4, 35
	s_mov_b32 s25, 0x41d80000
	s_mov_b32 s31, 0x426c0000
	v_writelane_b32 v249, s5, 36
	s_add_u32 s4, s2, 0x5200
	s_addc_u32 s5, s3, 0
	v_writelane_b32 v249, s4, 37
	s_mov_b32 s21, 0x42640000
	s_mov_b32 s35, 0x424c0000
	v_writelane_b32 v249, s5, 38
	s_add_u32 s4, s2, 0x5300
	s_addc_u32 s5, s3, 0
	v_writelane_b32 v249, s4, 39
	s_cmp_eq_u32 s33, 15
	s_mov_b32 s81, 0x42440000
	v_writelane_b32 v249, s5, 40
	s_cselect_b64 s[4:5], -1, 0
	v_writelane_b32 v249, s4, 41
	s_cmp_eq_u32 s33, 14
	s_mov_b32 s77, 0x422c0000
	v_writelane_b32 v249, s5, 42
	s_cselect_b64 s[4:5], -1, 0
	v_writelane_b32 v249, s4, 43
	s_cmp_eq_u32 s33, 13
	s_mov_b32 s83, 0x42240000
	v_writelane_b32 v249, s5, 44
	s_cselect_b64 s[4:5], -1, 0
	v_writelane_b32 v249, s4, 45
	s_cmp_eq_u32 s33, 12
	s_mov_b32 s85, 0x420c0000
	v_writelane_b32 v249, s5, 46
	s_cselect_b64 s[4:5], -1, 0
	v_writelane_b32 v249, s4, 47
	s_cmp_eq_u32 s33, 11
	s_mov_b32 s87, 0x42040000
	v_writelane_b32 v249, s5, 48
	s_cselect_b64 s[4:5], -1, 0
	v_writelane_b32 v249, s4, 49
	s_cmp_eq_u32 s33, 10
	v_mov_b32_e32 v229, -1
	v_writelane_b32 v249, s5, 50
	s_cselect_b64 s[4:5], -1, 0
	v_writelane_b32 v249, s4, 51
	s_cmp_eq_u32 s33, 9
	v_mov_b32_e32 v230, 0x3727c5ac
	v_writelane_b32 v249, s5, 52
	s_cselect_b64 s[4:5], -1, 0
	v_writelane_b32 v249, s4, 53
	s_cmp_eq_u32 s33, 8
	v_mov_b64_e32 v[194:195], 0xdbf
	v_writelane_b32 v249, s5, 54
	s_cselect_b64 s[4:5], -1, 0
	v_writelane_b32 v249, s4, 55
	s_cmp_eq_u32 s33, 7
	v_mov_b32_e32 v196, 0x3f317218
	v_writelane_b32 v249, s5, 56
	s_cselect_b64 s[4:5], -1, 0
	v_writelane_b32 v249, s4, 57
	s_cmp_eq_u32 s33, 6
	v_mov_b32_e32 v231, 0x7f800000
	v_writelane_b32 v249, s5, 58
	s_cselect_b64 s[4:5], -1, 0
	v_writelane_b32 v249, s4, 59
	s_cmp_eq_u32 s33, 5
	v_mov_b32_e32 v232, 0x7fc00000
	v_writelane_b32 v249, s5, 60
	s_cselect_b64 s[4:5], -1, 0
	v_writelane_b32 v249, s4, 61
	s_cmp_eq_u32 s33, 4
	v_mov_b32_e32 v233, 0xff800000
	v_writelane_b32 v249, s5, 62
	s_cselect_b64 s[4:5], -1, 0
	v_writelane_b32 v249, s4, 63
	s_cmp_eq_u32 s33, 3
	v_mov_b32_e32 v234, 0x42800000
	v_writelane_b32 v248, s5, 0
	s_cselect_b64 s[4:5], -1, 0
	v_writelane_b32 v248, s4, 1
	s_cmp_eq_u32 s33, 2
	v_mov_b64_e32 v[198:199], 0x1ff
	v_writelane_b32 v248, s5, 2
	s_cselect_b64 s[4:5], -1, 0
	v_writelane_b32 v248, s4, 3
	s_cmp_eq_u32 s33, 1
	s_mov_b32 s94, 0xbe800000
	v_writelane_b32 v248, s5, 4
	s_cselect_b64 s[4:5], -1, 0
	v_writelane_b32 v248, s4, 5
	s_cmp_eq_u32 s33, 0
	s_movk_i32 s95, 0x7fff
	v_writelane_b32 v248, s5, 6
	s_cselect_b64 s[4:5], -1, 0
	s_lshl_b32 s1, s33, 8
	v_writelane_b32 v248, s4, 7
	s_add_u32 s1, s14, s1
	s_movk_i32 s33, 0x6e00
	v_writelane_b32 v248, s5, 8
	s_addc_u32 s4, s15, 0
	s_add_u32 s8, s1, 0x1400
	s_addc_u32 s9, s4, 0
	v_writelane_b32 v248, s8, 9
	s_mov_b64 s[90:91], 0x80
	s_mov_b32 s96, 0xc1000000
	v_writelane_b32 v248, s9, 10
	s_add_u32 s8, s1, 0x2400
	s_addc_u32 s9, s4, 0
	v_writelane_b32 v248, s8, 11
	s_add_u32 s4, s2, 0x7400
	s_addc_u32 s5, s3, 0
	v_writelane_b32 v248, s9, 12
	v_writelane_b32 v248, s4, 13
	s_add_u32 s2, s2, 0x7500
	s_addc_u32 s3, s3, 0
	v_writelane_b32 v248, s5, 14
	v_writelane_b32 v248, s2, 15
; #define GAS __attribute__((address_space(1)))
; __device__ __forceinline__ void nsa_mfma_phase(Frame& F, int l, bf16* YC, int ypitch) {
;     ...
;     const int vcu = (F.G % 8 == 0) ? (F.bx % 8) * (F.G / 8) + F.bx / 8 : F.bx;
; template <unsigned PHMASK> __global__ void __launch_bounds__(NTHR, 2) fwd(Args args) {
;     ...
;             { int rv_[8]; bool ok_[8];
;               int tg = F.tid; asm volatile("" : "+v"(tg)); const int tc = tg < 256 ? tg : 0;
; #pragma unroll
;               for (int i = 0; i < 8; ++i) { pg8::Unit u; ok_[i] = S.next(i, u); const int e_ = ok_[i] ? u.e : 0; const int pos = (ok_[i] ? u.rb : 0) * 256 + tc; const bool in_ = ok_[i] && pos < mcnt[e_];
;                   rv_[i] = *(const GAS int*)(ldst + (size_t)e_ * T + (in_ ? pos : 0)); if (!in_) rv_[i] = 0; }
	s_nop 1
	v_writelane_b32 v248, s3, 16
	s_lshl_b64 s[2:3], s[92:93], 9
	v_writelane_b32 v248, s2, 17
	s_nop 1
	v_writelane_b32 v248, s3, 18
	s_lshl_b64 s[2:3], s[52:53], 9
	v_writelane_b32 v248, s2, 19
	s_cmpk_lt_i32 s92, 0x100
	s_nop 0
	v_writelane_b32 v248, s3, 20
	s_cselect_b64 s[2:3], -1, 0
	s_and_b32 s0, s0, -8
	s_ashr_i32 s1, s52, 3
	s_sub_i32 s8, s92, s0
	v_writelane_b32 v248, s2, 21
	s_mul_i32 s0, s1, s8
	s_add_i32 s1, s0, s7
	v_writelane_b32 v248, s3, 22
	s_lshl_b32 s13, s92, 3
	s_and_b32 s2, s52, 7
	s_lshl_b32 s38, s52, 3
	s_cmpk_lt_i32 s92, 0x200
	s_cselect_b64 s[4:5], -1, 0
	v_writelane_b32 v248, s4, 23
	s_not_b32 s0, s92
	s_ashr_i32 s9, s8, 31
	v_writelane_b32 v248, s5, 24
	s_add_i32 s0, s52, s0
	v_writelane_b32 v248, s0, 25
	s_lshl_b64 s[4:5], s[8:9], 20
	v_writelane_b32 v248, s4, 26
	s_lshl_b32 s3, s8, 6
	s_add_i32 s0, s38, 0x3fff
	v_writelane_b32 v248, s5, 27
	v_readlane_b32 s4, v249, 5
	v_readlane_b32 s5, v249, 6
	s_cmp_gt_i32 s5, 12
	s_cselect_b64 s[4:5], -1, 0
	v_writelane_b32 v248, s4, 28
	s_cmp_lt_i32 s8, 0
	s_mov_b32 s6, s8
	v_writelane_b32 v248, s5, 29
	s_mul_i32 s4, s8, 0x41
	s_cselect_b32 s3, s4, s3
	s_movk_i32 s4, 0x1b9
	s_cselect_b32 s4, s4, 0x1b8
	s_mul_i32 s4, s8, s4
	v_writelane_b32 v248, s6, 30
	s_add_i32 s4, s4, s7
	s_mul_hi_i32 s5, s4, 0x94f2095
	v_writelane_b32 v248, s7, 31
	s_lshr_b32 s6, s5, 31
	s_ashr_i32 s5, s5, 4
	s_add_i32 s5, s5, s6
	s_mul_i32 s6, s5, 0x1b8
	s_lshl_b32 s5, s5, 3
	s_sub_i32 s4, s4, s6
	s_sub_i32 s6, 64, s5
	s_min_i32 s6, s6, 8
	s_cmp_eq_u32 s2, 0
	s_cselect_b32 s1, s1, s92
	s_cmpk_lt_i32 s1, 0x400
	s_cselect_b64 s[8:9], -1, 0
	s_add_i32 s11, s52, s92
	v_writelane_b32 v248, s1, 32
	s_ashr_i32 s10, s11, 31
	v_writelane_b32 v248, s8, 33
	s_lshr_b32 s10, s10, 29
	s_add_i32 s10, s11, s10
	v_writelane_b32 v248, s9, 34
	v_writelane_b32 v248, s7, 35
	s_ashr_i32 s10, s10, 3
	v_writelane_b32 v248, s10, 36
	v_writelane_b32 v248, s11, 37
	s_add_i32 s11, s11, s52
	s_ashr_i32 s10, s11, 31
	s_lshr_b32 s10, s10, 29
	s_add_i32 s10, s11, s10
	s_ashr_i32 s10, s10, 3
	v_writelane_b32 v248, s10, 38
	v_writelane_b32 v248, s11, 39
	s_add_i32 s11, s11, s52
	s_ashr_i32 s10, s11, 31
	s_lshr_b32 s10, s10, 29
	s_add_i32 s10, s11, s10
	s_add_i32 s1, s3, s7
	s_ashr_i32 s10, s10, 3
	s_ashr_i32 s2, s1, 31
	v_writelane_b32 v248, s10, 40
	s_lshr_b32 s2, s2, 26
	v_writelane_b32 v248, s11, 41
	s_add_i32 s11, s11, s52
	s_add_i32 s2, s1, s2
	s_ashr_i32 s10, s11, 31
	s_and_b32 s3, s2, 0xffffffc0
	s_lshr_b32 s10, s10, 29
	s_sub_i32 s1, s1, s3
	s_abs_i32 s3, s6
	s_add_i32 s10, s11, s10
	v_cvt_f32_u32_e32 v0, s3
	s_ashr_i32 s10, s10, 3
	v_writelane_b32 v248, s10, 42
	v_writelane_b32 v248, s11, 43
	s_add_i32 s11, s11, s52
	s_ashr_i32 s10, s11, 31
	v_rcp_iflag_f32_e32 v0, v0
	s_lshr_b32 s10, s10, 29
	s_add_i32 s10, s11, s10
	s_ashr_i32 s10, s10, 3
	v_writelane_b32 v248, s10, 44
	v_mul_f32_e32 v0, 0x4f7ffffe, v0
	v_writelane_b32 v248, s11, 45
	s_add_i32 s11, s11, s52
	v_cvt_u32_f32_e32 v0, v0
	s_ashr_i32 s10, s11, 31
	s_lshr_b32 s10, s10, 29
	s_add_i32 s10, s11, s10
	s_ashr_i32 s10, s10, 3
	s_sub_i32 s7, 0, s3
	v_readfirstlane_b32 s8, v0
	v_writelane_b32 v248, s10, 46
	s_mul_i32 s7, s7, s8
	v_writelane_b32 v248, s11, 47
	s_add_i32 s11, s11, s52
	s_mul_hi_u32 s7, s8, s7
	s_ashr_i32 s10, s11, 31
	s_add_i32 s8, s8, s7
	s_abs_i32 s7, s4
	s_lshr_b32 s10, s10, 29
	s_mul_hi_u32 s8, s7, s8
	s_ashr_i32 s2, s2, 6
	s_add_i32 s10, s11, s10
	s_mul_i32 s9, s8, s3
	s_lshl_b32 s2, s2, 3
	v_writelane_b32 v248, s11, 48
	s_ashr_i32 s10, s10, 3
	s_sub_i32 s7, s7, s9
	s_sub_i32 s9, 64, s2
	v_writelane_b32 v248, s10, 49
	s_xor_b32 s10, s4, s6
	s_min_i32 s9, s9, 8
	s_ashr_i32 s10, s10, 31
	s_add_i32 s11, s8, 1
	s_sub_i32 s12, s7, s3
	s_cmp_ge_u32 s7, s3
	s_cselect_b32 s8, s11, s8
	s_cselect_b32 s7, s12, s7
	s_add_i32 s11, s8, 1
	s_cmp_ge_u32 s7, s3
	s_cselect_b32 s3, s11, s8
	s_xor_b32 s3, s3, s10
	s_sub_i32 s3, s3, s10
	v_writelane_b32 v248, s3, 50
	s_mul_i32 s3, s3, s6
	s_sub_i32 s3, s4, s3
	s_add_i32 s3, s5, s3
	v_writelane_b32 v248, s3, 51
	s_abs_i32 s3, s9
	v_cvt_f32_u32_e32 v0, s3
	s_sub_i32 s4, 0, s3
	v_writelane_b32 v248, s16, 52
	v_rcp_iflag_f32_e32 v0, v0
	s_nop 0
	v_writelane_b32 v248, s17, 53
	v_cndmask_b32_e64 v222, 0, 1, s[16:17]
	s_mov_b32 s17, 0xff800000
	v_mul_f32_e32 v0, 0x4f7ffffe, v0
	v_cvt_u32_f32_e32 v0, v0
	s_nop 0
	v_readfirstlane_b32 s5, v0
	s_mul_i32 s4, s4, s5
	s_mul_hi_u32 s4, s5, s4
	s_add_i32 s5, s5, s4
	s_abs_i32 s4, s1
	s_mul_hi_u32 s5, s4, s5
	s_mul_i32 s6, s5, s3
	s_sub_i32 s4, s4, s6
	s_xor_b32 s6, s1, s9
	s_ashr_i32 s6, s6, 31
	s_add_i32 s7, s5, 1
	s_sub_i32 s8, s4, s3
	s_cmp_ge_u32 s4, s3
	s_cselect_b32 s5, s7, s5
	s_cselect_b32 s4, s8, s4
	s_add_i32 s7, s5, 1
	s_cmp_ge_u32 s4, s3
	s_cselect_b32 s3, s7, s5
	s_xor_b32 s3, s3, s6
	s_sub_i32 s8, s3, s6
	s_mul_i32 s3, s8, s9
	s_sub_i32 s1, s1, s3
	s_abs_i32 s3, s38
	v_cvt_f32_u32_e32 v0, s3
	s_sub_i32 s4, 0, s3
	s_ashr_i32 s9, s8, 31
	s_lshl_b64 s[14:15], s[8:9], 20
	v_rcp_iflag_f32_e32 v0, v0
	s_nop 0
	v_mul_f32_e32 v0, 0x4f7ffffe, v0
	v_cvt_u32_f32_e32 v0, v0
	s_nop 0
	v_readfirstlane_b32 s5, v0
	s_mul_i32 s4, s4, s5
	s_mul_hi_u32 s4, s5, s4
	s_add_i32 s5, s5, s4
	s_abs_i32 s4, s0
	s_mul_hi_u32 s5, s4, s5
	s_mul_i32 s6, s5, s3
	s_sub_i32 s4, s4, s6
	s_add_i32 s6, s2, s1
	s_ashr_i32 s7, s6, 31
	s_xor_b32 s0, s0, s38
	s_ashr_i32 s0, s0, 31
	s_add_i32 s1, s5, 1
	s_sub_i32 s2, s4, s3
	s_lshl_b64 s[10:11], s[6:7], 20
	s_cmp_ge_u32 s4, s3
	s_cselect_b32 s1, s1, s5
	s_cselect_b32 s2, s2, s4
	s_add_i32 s4, s1, 1
	s_cmp_ge_u32 s2, s3
	s_cselect_b32 s1, s4, s1
	s_xor_b32 s1, s1, s0
	s_sub_i32 s2, s1, s0
	s_cmp_gt_i32 s2, 0
	s_cselect_b64 s[0:1], -1, 0
	v_writelane_b32 v248, s0, 54
; #define GAS __attribute__((address_space(1)))
; template <unsigned PHMASK> __global__ void __launch_bounds__(NTHR, 2) fwd(Args args) {
;     ...
;         if ((PHON(9) || PHON(10)) && (IN(pb + 8) || IN(pb + 9))) { const int nu = __builtin_amdgcn_readfirstlane(mblk[16]) * 8; moe_heavy = (nu % F.G != 0) && (F.bx < nu % F.G); moe_q = nu / F.G; moe_h = nu % F.G; }
;         if (PHON(9) && IN(pb + 8)) for (int dup_ = 0; dup_ < (DUP_PHASE == 9 ? 2 : 1); ++dup_) { PHASE_FENCE();
;             pg8::MoeOrder S; S.A = (const char*)(F.ws + WS_X1B); S.B = (const char*)(lw + LW_GU); S.tstepA = 0; S.tstepB = (size_t)256 * DM * 2; S.estepB = (size_t)2048 * DM * 2;
;             S.blk_start = mblk; S.rows = mrows; S.nN = 8; S.G = F.G; S.c = F.bx;
;             { int rv_[8]; bool ok_[8];
;               int tg = F.tid; asm volatile("" : "+v"(tg)); const int tc = tg < 256 ? tg : 0;
; #pragma unroll
;               for (int i = 0; i < 8; ++i) { pg8::Unit u; ok_[i] = S.next(i, u); const int e_ = ok_[i] ? u.e : 0; const int pos = (ok_[i] ? u.rb : 0) * 256 + tc; const bool in_ = ok_[i] && pos < mcnt[e_];
;                   rv_[i] = *(const GAS int*)(ldst + (size_t)e_ * T + (in_ ? pos : 0)); if (!in_) rv_[i] = 0; }
;     ...
;             S.blk_start = mblk; S.rows = nullptr; S.nN = 8; S.G = F.G; S.c = F.G - 1 - F.bx;
;             if (moe_h > 0 && 2 * moe_h <= F.G && moe_q >= 1) { S.nfull = moe_q - 1; S.G2 = F.G - moe_h; S.c2 = F.bx >= moe_h ? F.bx - moe_h : -1; }
	s_ashr_i32 s39, s38, 31
	s_nop 0
	v_writelane_b32 v248, s1, 55
	s_abs_i32 s0, s52
	v_cvt_f32_u32_e32 v0, s0
	v_writelane_b32 v248, s0, 56
	s_sub_i32 s0, 0, s0
	v_rcp_iflag_f32_e32 v0, v0
	s_nop 0
	v_mul_f32_e32 v0, 0x4f7ffffe, v0
	v_cvt_u32_f32_e32 v0, v0
	s_nop 0
	v_readfirstlane_b32 s1, v0
	s_mul_i32 s0, s0, s1
	s_mul_hi_u32 s0, s1, s0
	s_add_i32 s0, s1, s0
	v_writelane_b32 v248, s0, 57
	s_lshl_b32 s0, s6, 8
	v_writelane_b32 v248, s0, 58
	s_lshl_b32 s0, s8, 8
	v_writelane_b32 v248, s0, 59
	s_lshl_b32 s0, s92, 9
	v_writelane_b32 v248, s0, 60
	s_lshl_b32 s0, s52, 9
	v_writelane_b32 v248, s0, 61
	s_lshl_b32 s0, s92, 7
	v_writelane_b32 v248, s0, 62
	s_lshl_b32 s0, s52, 7
	v_writelane_b32 v248, s0, 63
	s_mov_b32 s0, s6
	v_writelane_b32 v247, s0, 0
	v_mbcnt_lo_u32_b32 v0, -1, 0
	s_nop 0
	v_writelane_b32 v247, s1, 1
	s_lshl_b64 s[0:1], s[6:7], 17
	v_writelane_b32 v247, s0, 2
	v_mbcnt_hi_u32_b32 v228, -1, v0
	s_movk_i32 s6, 0x1800
	v_writelane_b32 v247, s1, 3
	s_mov_b32 s0, s8
	v_writelane_b32 v247, s0, 4
	s_nop 1
	v_writelane_b32 v247, s1, 5
	s_lshl_b64 s[0:1], s[8:9], 17
	v_writelane_b32 v247, s0, 6
	s_mov_b32 s8, s89
	s_nop 0
	v_writelane_b32 v247, s1, 7
	s_lshl_b64 s[0:1], s[92:93], 12
	v_writelane_b32 v247, s0, 8
	s_nop 1
	v_writelane_b32 v247, s1, 9
	s_lshl_b64 s[0:1], s[52:53], 12
	v_writelane_b32 v247, s0, 10
	s_nop 1
	v_writelane_b32 v247, s1, 11
	s_lshl_b64 s[0:1], s[38:39], 2
	v_writelane_b32 v247, s0, 12
	s_nop 1
	v_writelane_b32 v247, s1, 13
	s_add_u32 s0, s14, 0x11b00100
	v_writelane_b32 v247, s0, 14
	v_writelane_b32 v247, s14, 15
	s_addc_u32 s0, s15, 0
	s_nop 0
	v_writelane_b32 v247, s15, 16
	v_writelane_b32 v247, s0, 17
	s_add_u32 s0, s10, 0x6a880080
	s_addc_u32 s1, s11, 0
	v_writelane_b32 v247, s0, 18
	s_movk_i32 s15, 0x200
	s_mov_b32 s14, 0x3fb504f3
	v_writelane_b32 v247, s1, 19
	s_add_u32 s0, s10, 0x6a800100
	v_writelane_b32 v247, s10, 20
	s_addc_u32 s1, s11, 0
	s_add_i32 s7, 0, 0x14400
	v_writelane_b32 v247, s11, 21
	v_writelane_b32 v247, s0, 22
	s_nop 1
	v_writelane_b32 v247, s1, 23
	s_ashr_i32 s0, s13, 31
	v_writelane_b32 v247, s0, 24
	v_writelane_b32 v247, s13, 25
	s_add_i32 s0, s38, s13
	v_writelane_b32 v247, s0, 26
	v_writelane_b32 v247, s52, 27
	s_lshl_b32 s0, s52, 4
	s_nop 0
	v_writelane_b32 v247, s53, 28
	v_writelane_b32 v247, s0, 29
	s_add_i32 s0, 0, 0x231d8
	v_writelane_b32 v247, s0, 30
	s_add_i32 s0, 0, 0x23020
	v_writelane_b32 v247, s0, 31
	s_add_i32 s0, 0, 0x23024
	v_writelane_b32 v247, s0, 32
	s_add_i32 s0, 0, 0x23118
	v_writelane_b32 v247, s0, 33
	s_add_i32 s0, 0, 0x23128
	v_writelane_b32 v247, s0, 34
	s_add_i32 s0, 0, 0x23140
	v_writelane_b32 v247, s0, 35
	s_add_i32 s0, 0, 0x23150
	v_writelane_b32 v247, s0, 36
	s_add_i32 s0, 0, 0xc400
	v_writelane_b32 v247, s0, 37
	s_add_i32 s0, 0, 0x1d400
	v_writelane_b32 v247, s0, 38
	s_add_i32 s0, 0, 0x1d800
	v_writelane_b32 v247, s0, 39
	s_add_i32 s0, 0, 0x1e400
	v_writelane_b32 v247, s0, 40
	s_add_i32 s0, 0, 0x1dc00
	v_writelane_b32 v247, s0, 41
	s_add_i32 s0, 0, 0x16980
	v_writelane_b32 v247, s0, 42
	s_add_i32 s0, 0, 0x23190
	v_writelane_b32 v247, s0, 43
	s_add_i32 s0, 0, 0x231a0
	v_writelane_b32 v247, s0, 44
	s_add_i32 s0, 0, 0x20600
	v_writelane_b32 v247, s0, 45
	s_add_i32 s0, 0, 0x20640
	v_writelane_b32 v247, s0, 46
	s_add_i32 s0, 0, 0x20200
	v_writelane_b32 v247, s0, 47
	s_add_i32 s0, 0, 0x20400
	v_writelane_b32 v247, s0, 48
	s_add_i32 s0, 0, 0x20080
	v_writelane_b32 v247, s0, 49
	s_add_i32 s0, 0, 0x20044
	v_writelane_b32 v247, s0, 50
	s_add_i32 s0, 0, 0x2004c
	v_writelane_b32 v247, s0, 51
	s_add_i32 s0, 0, 0x20054
	v_writelane_b32 v247, s0, 52
	s_add_i32 s0, 0, 0x2005c
	v_writelane_b32 v247, s0, 53
	s_add_i32 s0, 0, 0x20064
	v_writelane_b32 v247, s0, 54
	s_add_i32 s0, 0, 0x2006c
	v_writelane_b32 v247, s0, 55
	s_add_i32 s0, 0, 0x20074
	v_writelane_b32 v247, s0, 56
	s_add_i32 s0, 0, 0x2007c
	v_writelane_b32 v247, s0, 57
	s_add_i32 s0, 0, 0x20100
	v_writelane_b32 v247, s0, 58
	s_add_i32 s0, 0, 0x231d0
	v_writelane_b32 v247, s0, 59
	s_lshl_b64 s[0:1], s[38:39], 12
	v_writelane_b32 v247, s0, 60
	s_nop 1
	v_writelane_b32 v247, s1, 61
	s_mov_b32 s0, s38
	v_writelane_b32 v247, s0, 62
	s_nop 1
	v_writelane_b32 v247, s1, 63
	s_lshl_b64 s[0:1], s[38:39], 13
	v_writelane_b32 v246, s0, 0
	s_nop 1
	v_writelane_b32 v246, s1, 1
	s_mov_b64 s[0:1], -1
	v_writelane_b32 v246, s0, 2
	s_nop 1
	v_writelane_b32 v246, s1, 3
	v_writelane_b32 v246, s92, 4
	s_nop 1
	v_writelane_b32 v246, s93, 5
	v_writelane_b32 v246, s2, 6
	v_readlane_b32 s100, v248, 32
	s_nop 1
	s_not_b32 s101, s100
	s_add_i32 s101, s52, s101
	v_writelane_b32 v248, s101, 25
	s_nop 1
	s_and_b32 s101, s100, 7
	v_writelane_b32 v248, s101, 30
	s_nop 1
	s_lshl_b32 s101, s101, 20
	v_writelane_b32 v248, s101, 26
	s_nop 1
	s_mov_b32 s101, 0
	v_writelane_b32 v248, s101, 27
	s_nop 1
	s_lshr_b32 s101, s100, 3
	v_writelane_b32 v248, s101, 31
	s_nop 1
	v_writelane_b32 v248, s101, 35
	s_nop 1
	s_mov_b32 vcc_lo, s100
	s_add_i32 vcc_lo, vcc_lo, s52
	s_ashr_i32 s101, vcc_lo, 3
	v_writelane_b32 v248, vcc_lo, 37
	s_nop 1
	v_writelane_b32 v248, s101, 36
	s_nop 1
	s_add_i32 vcc_lo, vcc_lo, s52
	s_ashr_i32 s101, vcc_lo, 3
	v_writelane_b32 v248, vcc_lo, 39
	s_nop 1
	v_writelane_b32 v248, s101, 38
	s_nop 1
	s_add_i32 vcc_lo, vcc_lo, s52
	s_ashr_i32 s101, vcc_lo, 3
	v_writelane_b32 v248, vcc_lo, 41
	s_nop 1
	v_writelane_b32 v248, s101, 40
	s_nop 1
	s_add_i32 vcc_lo, vcc_lo, s52
	s_ashr_i32 s101, vcc_lo, 3
	v_writelane_b32 v248, vcc_lo, 43
	s_nop 1
	v_writelane_b32 v248, s101, 42
	s_nop 1
	s_add_i32 vcc_lo, vcc_lo, s52
	s_ashr_i32 s101, vcc_lo, 3
	v_writelane_b32 v248, vcc_lo, 45
	s_nop 1
	v_writelane_b32 v248, s101, 44
	s_nop 1
	s_add_i32 vcc_lo, vcc_lo, s52
	s_ashr_i32 s101, vcc_lo, 3
	v_writelane_b32 v248, vcc_lo, 47
	s_nop 1
	v_writelane_b32 v248, s101, 46
	s_nop 1
	s_add_i32 vcc_lo, vcc_lo, s52
	s_ashr_i32 s101, vcc_lo, 3
	v_writelane_b32 v248, vcc_lo, 48
	s_nop 1
	v_writelane_b32 v248, s101, 49
	s_nop 1
	s_branch .LBB0_206

; #define PG8_STAGE_A(bufoff, kptr, h) do { if constexpr (GATHER) { PG8_STAGE(bufoff, kptr, oa[h]); } else { PG8_STAGE(bufoff, (kptr) + (h) * hstep, voffA); } } while (0)
; #define PG8_GATHER_OFFS(uidx) do { _Pragma("unroll") for (int _h = 0; _h < 2; ++_h) _Pragma("unroll") for (int _i = 0; _i < 2; ++_i) \
;         oa[_h][_i] = (unsigned)(S.gather_row((uidx), _h * HALF + _i * 64 + Rst0) * K + Cst0) * 2u; } while (0)
; #define PG8_STAGE(bufoff, gbase, voff) do { _Pragma("unroll") for (int _i = 0; _i < 2; ++_i) \
;         __builtin_amdgcn_global_load_lds((const unsigned*)((const char*)(gbase) + (voff)[_i]), (LAS unsigned*)(lds + (bufoff) + ldsw + _i * 8192), 16, 0, 0); } while (0)
; #define PG8_LDA(dst, b, h) do { _Pragma("unroll") for (int m = 0; m < 4; ++m) _Pragma("unroll") for (int k = 0; k < 2; ++k) dst[m][k] = *(const LAS bf16x8*)(lds + PG8_SA(b, h) + aoff + m * 2048 + k * 1024); } while (0)
; #define PG8_LDB(dst, b, h) do { _Pragma("unroll") for (int n = 0; n < 2; ++n) _Pragma("unroll") for (int k = 0; k < 2; ++k) dst[n][k] = *(const LAS bf16x8*)(lds + PG8_SB(b, h) + boff + n * 2048 + k * 1024); } while (0)
; #define PG8_MMA(ai, bj, At, Bt) do { __builtin_amdgcn_s_setprio(1); _Pragma("unroll") for (int m = 0; m < 4; ++m) _Pragma("unroll") for (int n = 0; n < 2; ++n) _Pragma("unroll") for (int k = 0; k < 2; ++k) \
;         acc[ai][bj][m][n] = __builtin_amdgcn_mfma_f32_16x16x32_bf16(Bt[n][k], At[m][k], acc[ai][bj][m][n], 0, 0, 0); __builtin_amdgcn_s_setprio(0); } while (0)
; #define PG8_WAIT_V(n) asm volatile("s_waitcnt vmcnt(" #n ")" ::: "memory")
; template <class Epi, class Sched, bool GATHER, bool SEGHOOK = false>
; __device__ __forceinline__ void gemm_phase(LAS unsigned char* lds, const int K, const Sched& S, const Epi& E, int tid_) {
;     ...
;             PG8_LDB(B0, 0, 0); PG8_LDB(B1, 0, 1); PG8_SCHED; PG8_LDA(At, 0, 0); PG8_STAGE_A(PG8_SA(1, 1), a1, 1);
;             if constexpr (GATHER) { if (last && has_next) { PG8_GATHER_OFFS(ui + 1); } }
;             PG8_WAIT_V(8); PG8_WAIT_L(0); PG8_BAR; PG8_MMA(0, 0, At, B0); PG8_MMA(0, 1, At, B1); PG8_BAR; PG8_SCHED;
;             PG8_LDA(At, 0, 1); PG8_STAGE(PG8_SB(0, 0), b2, voffB); PG8_STAGE(PG8_SB(0, 1), b2 + hstep, voffB); PG8_STAGE_A(PG8_SA(0, 0), a2, 0);
;             PG8_WAIT_V(8); PG8_WAIT_L(0); PG8_BAR; PG8_MMA(1, 0, At, B0); PG8_MMA(1, 1, At, B1); PG8_BAR; PG8_SCHED;
.LBB0_219:
	s_add_u32 s9, s50, 0xfff80080
	s_addc_u32 s52, s51, -1
	s_add_i32 s71, 0, 0x10000
	s_cmp_eq_u32 s70, 28
	s_cselect_b32 s55, s8, s52
	s_cselect_b32 s54, s16, s9
	s_cselect_b32 s53, s13, s69
	s_cselect_b32 s52, s39, s41
	s_add_i32 s9, 0, 0x14000
	v_add_u32_e32 v156, s71, v145
	v_add_u32_e32 v172, s9, v145
	v_lshl_add_u64 v[192:193], s[50:51], 0, v[138:139]
	s_add_i32 m0, s49, 0xc000
	s_nop 0
	global_load_lds_dwordx4 v[192:193], off
	v_lshl_add_u64 v[192:193], s[50:51], 0, v[136:137]
	s_add_i32 m0, s49, 0xe000
	s_nop 0
	global_load_lds_dwordx4 v[192:193], off
	ds_read_b128 v[140:143], v156
	ds_read_b128 v[148:151], v156 offset:1024
	ds_read_b128 v[152:155], v156 offset:2048
	ds_read_b128 v[156:159], v156 offset:3072
	ds_read_b128 v[160:163], v172
	ds_read_b128 v[164:167], v172 offset:1024
	ds_read_b128 v[168:171], v172 offset:2048
	ds_read_b128 v[172:175], v172 offset:3072
	ds_read_b128 v[176:179], v147
	ds_read_b128 v[180:183], v147 offset:1024
	ds_read_b128 v[184:187], v147 offset:2048
	ds_read_b128 v[188:191], v147 offset:3072
	ds_read_b128 v[200:203], v147 offset:4096
	ds_read_b128 v[204:207], v147 offset:5120
	ds_read_b128 v[208:211], v147 offset:6144
	ds_read_b128 v[212:215], v147 offset:7168
	s_waitcnt vmcnt(8)
	s_waitcnt lgkmcnt(0)
	s_barrier
	s_setprio 1
	s_waitcnt lgkmcnt(0)
	v_mfma_f32_16x16x32_bf16 v[126:129], v[140:143], v[176:179], v[126:129]
	v_mfma_f32_16x16x32_bf16 v[122:125], v[152:155], v[176:179], v[122:125]
	v_mfma_f32_16x16x32_bf16 v[110:113], v[140:143], v[184:187], v[110:113]
	v_mfma_f32_16x16x32_bf16 v[106:109], v[152:155], v[184:187], v[106:109]
	v_mfma_f32_16x16x32_bf16 v[94:97], v[140:143], v[200:203], v[94:97]
	v_mfma_f32_16x16x32_bf16 v[90:93], v[152:155], v[200:203], v[90:93]
	v_mfma_f32_16x16x32_bf16 v[78:81], v[140:143], v[208:211], v[78:81]
	v_mfma_f32_16x16x32_bf16 v[74:77], v[152:155], v[208:211], v[74:77]
	v_mfma_f32_16x16x32_bf16 v[126:129], v[148:151], v[180:183], v[126:129]
	v_mfma_f32_16x16x32_bf16 v[122:125], v[156:159], v[180:183], v[122:125]
	v_mfma_f32_16x16x32_bf16 v[110:113], v[148:151], v[188:191], v[110:113]
	v_mfma_f32_16x16x32_bf16 v[106:109], v[156:159], v[188:191], v[106:109]
	v_mfma_f32_16x16x32_bf16 v[94:97], v[148:151], v[204:207], v[94:97]
	v_mfma_f32_16x16x32_bf16 v[90:93], v[156:159], v[204:207], v[90:93]
	v_mfma_f32_16x16x32_bf16 v[78:81], v[148:151], v[212:215], v[78:81]
	v_mfma_f32_16x16x32_bf16 v[74:77], v[156:159], v[212:215], v[74:77]
	s_setprio 0
	s_setprio 1
	v_mfma_f32_16x16x32_bf16 v[118:121], v[160:163], v[176:179], v[118:121]
	v_mfma_f32_16x16x32_bf16 v[114:117], v[168:171], v[176:179], v[114:117]
	v_mfma_f32_16x16x32_bf16 v[102:105], v[160:163], v[184:187], v[102:105]
	v_mfma_f32_16x16x32_bf16 v[98:101], v[168:171], v[184:187], v[98:101]
	v_mfma_f32_16x16x32_bf16 v[86:89], v[160:163], v[200:203], v[86:89]
	v_mfma_f32_16x16x32_bf16 v[82:85], v[168:171], v[200:203], v[82:85]
	v_mfma_f32_16x16x32_bf16 v[70:73], v[160:163], v[208:211], v[70:73]
	v_mfma_f32_16x16x32_bf16 v[66:69], v[168:171], v[208:211], v[66:69]
	v_mfma_f32_16x16x32_bf16 v[118:121], v[164:167], v[180:183], v[118:121]
	v_mfma_f32_16x16x32_bf16 v[114:117], v[172:175], v[180:183], v[114:117]
	v_mfma_f32_16x16x32_bf16 v[102:105], v[164:167], v[188:191], v[102:105]
	v_mfma_f32_16x16x32_bf16 v[98:101], v[172:175], v[188:191], v[98:101]
	v_mfma_f32_16x16x32_bf16 v[86:89], v[164:167], v[204:207], v[86:89]
	v_mfma_f32_16x16x32_bf16 v[82:85], v[172:175], v[204:207], v[82:85]
	v_mfma_f32_16x16x32_bf16 v[70:73], v[164:167], v[212:215], v[70:73]
	v_mfma_f32_16x16x32_bf16 v[66:69], v[172:175], v[212:215], v[66:69]
	s_setprio 0
	s_barrier
	s_add_i32 s71, s71, s62
	v_lshl_add_u64 v[192:193], s[52:53], 0, v[0:1]
	s_mov_b32 m0, s71
	s_nop 0
	global_load_lds_dwordx4 v[192:193], off
	s_add_i32 m0, s71, 0x2000
	s_add_u32 s78, s52, 0x80000
	v_lshl_add_u64 v[216:217], s[52:53], 0, v[134:135]
	s_addc_u32 s79, s53, 0
	s_add_i32 s9, s9, s62
	global_load_lds_dwordx4 v[216:217], off
	v_lshl_add_u64 v[218:219], s[78:79], 0, v[0:1]
	s_mov_b32 m0, s9
	v_lshl_add_u64 v[220:221], s[54:55], 0, v[132:133]
	global_load_lds_dwordx4 v[218:219], off
	v_lshl_add_u64 v[218:219], s[78:79], 0, v[134:135]
	s_add_i32 m0, s9, 0x2000
	s_nop 0
	global_load_lds_dwordx4 v[218:219], off
	v_lshl_add_u64 v[218:219], s[54:55], 0, v[130:131]
	s_mov_b32 m0, s49
	s_nop 0
	global_load_lds_dwordx4 v[218:219], off
	s_mov_b32 m0, s63
	s_nop 0
	global_load_lds_dwordx4 v[220:221], off
	ds_read_b128 v[176:179], v147 offset:16384
	ds_read_b128 v[180:183], v147 offset:17408
	ds_read_b128 v[184:187], v147 offset:18432
	ds_read_b128 v[188:191], v147 offset:19456
	ds_read_b128 v[200:203], v147 offset:20480
	ds_read_b128 v[204:207], v147 offset:21504
	ds_read_b128 v[208:211], v147 offset:22528
	ds_read_b128 v[212:215], v147 offset:23552
	s_waitcnt vmcnt(8)
	s_waitcnt lgkmcnt(0)
	s_barrier
; #define PG8_STAGE_A(bufoff, kptr, h) do { if constexpr (GATHER) { PG8_STAGE(bufoff, kptr, oa[h]); } else { PG8_STAGE(bufoff, (kptr) + (h) * hstep, voffA); } } while (0)
; #define PG8_LDA(dst, b, h) do { _Pragma("unroll") for (int m = 0; m < 4; ++m) _Pragma("unroll") for (int k = 0; k < 2; ++k) dst[m][k] = *(const LAS bf16x8*)(lds + PG8_SA(b, h) + aoff + m * 2048 + k * 1024); } while (0)
; #define PG8_LDB(dst, b, h) do { _Pragma("unroll") for (int n = 0; n < 2; ++n) _Pragma("unroll") for (int k = 0; k < 2; ++k) dst[n][k] = *(const LAS bf16x8*)(lds + PG8_SB(b, h) + boff + n * 2048 + k * 1024); } while (0)
; #define PG8_MMA(ai, bj, At, Bt) do { __builtin_amdgcn_s_setprio(1); _Pragma("unroll") for (int m = 0; m < 4; ++m) _Pragma("unroll") for (int n = 0; n < 2; ++n) _Pragma("unroll") for (int k = 0; k < 2; ++k) \
;         acc[ai][bj][m][n] = __builtin_amdgcn_mfma_f32_16x16x32_bf16(Bt[n][k], At[m][k], acc[ai][bj][m][n], 0, 0, 0); __builtin_amdgcn_s_setprio(0); } while (0)
; #define PG8_WAIT_V(n) asm volatile("s_waitcnt vmcnt(" #n ")" ::: "memory")
; #define PG8_WAIT_L(n) asm volatile("s_waitcnt lgkmcnt(" #n ")" ::: "memory")
; #define PG8_BAR __builtin_amdgcn_s_barrier()
; #define PG8_SCHED __builtin_amdgcn_sched_barrier(0)
; template <class Epi, class Sched, bool GATHER, bool SEGHOOK = false>
; __device__ __forceinline__ void gemm_phase(LAS unsigned char* lds, const int K, const Sched& S, const Epi& E, int tid_) {
;     ...
;             PG8_WAIT_V(8); PG8_WAIT_L(0); PG8_BAR; PG8_MMA(1, 0, At, B0); PG8_MMA(1, 1, At, B1); PG8_BAR; PG8_SCHED;
;             PG8_LDB(B0, 1, 0); PG8_LDB(B1, 1, 1); PG8_SCHED; PG8_LDA(At, 1, 0); PG8_STAGE_A(PG8_SA(0, 1), a2, 1);
;             PG8_WAIT_V(8); PG8_WAIT_L(0); PG8_BAR; PG8_MMA(0, 0, At, B0); PG8_MMA(0, 1, At, B1); PG8_BAR; PG8_SCHED;
	s_setprio 1
	s_waitcnt lgkmcnt(0)
	v_mfma_f32_16x16x32_bf16 v[62:65], v[140:143], v[176:179], v[62:65]
	v_mfma_f32_16x16x32_bf16 v[58:61], v[152:155], v[176:179], v[58:61]
	v_mfma_f32_16x16x32_bf16 v[46:49], v[140:143], v[184:187], v[46:49]
	v_mfma_f32_16x16x32_bf16 v[42:45], v[152:155], v[184:187], v[42:45]
	v_mfma_f32_16x16x32_bf16 v[30:33], v[140:143], v[200:203], v[30:33]
	v_mfma_f32_16x16x32_bf16 v[26:29], v[152:155], v[200:203], v[26:29]
	v_mfma_f32_16x16x32_bf16 v[14:17], v[140:143], v[208:211], v[14:17]
	v_mfma_f32_16x16x32_bf16 v[10:13], v[152:155], v[208:211], v[10:13]
	v_mfma_f32_16x16x32_bf16 v[62:65], v[148:151], v[180:183], v[62:65]
	v_mfma_f32_16x16x32_bf16 v[58:61], v[156:159], v[180:183], v[58:61]
	v_mfma_f32_16x16x32_bf16 v[46:49], v[148:151], v[188:191], v[46:49]
	v_mfma_f32_16x16x32_bf16 v[42:45], v[156:159], v[188:191], v[42:45]
	v_mfma_f32_16x16x32_bf16 v[30:33], v[148:151], v[204:207], v[30:33]
	v_mfma_f32_16x16x32_bf16 v[26:29], v[156:159], v[204:207], v[26:29]
	v_mfma_f32_16x16x32_bf16 v[14:17], v[148:151], v[212:215], v[14:17]
	v_mfma_f32_16x16x32_bf16 v[10:13], v[156:159], v[212:215], v[10:13]
	s_setprio 0
	s_setprio 1
	v_mfma_f32_16x16x32_bf16 v[54:57], v[160:163], v[176:179], v[54:57]
	v_mfma_f32_16x16x32_bf16 v[50:53], v[168:171], v[176:179], v[50:53]
	v_mfma_f32_16x16x32_bf16 v[38:41], v[160:163], v[184:187], v[38:41]
	v_mfma_f32_16x16x32_bf16 v[34:37], v[168:171], v[184:187], v[34:37]
	v_mfma_f32_16x16x32_bf16 v[22:25], v[160:163], v[200:203], v[22:25]
	v_mfma_f32_16x16x32_bf16 v[18:21], v[168:171], v[200:203], v[18:21]
	v_mfma_f32_16x16x32_bf16 v[6:9], v[160:163], v[208:211], v[6:9]
	v_mfma_f32_16x16x32_bf16 v[2:5], v[168:171], v[208:211], v[2:5]
	v_mfma_f32_16x16x32_bf16 v[54:57], v[164:167], v[180:183], v[54:57]
	v_mfma_f32_16x16x32_bf16 v[50:53], v[172:175], v[180:183], v[50:53]
	v_mfma_f32_16x16x32_bf16 v[38:41], v[164:167], v[188:191], v[38:41]
	v_mfma_f32_16x16x32_bf16 v[34:37], v[172:175], v[188:191], v[34:37]
	v_mfma_f32_16x16x32_bf16 v[22:25], v[164:167], v[204:207], v[22:25]
	v_mfma_f32_16x16x32_bf16 v[18:21], v[172:175], v[204:207], v[18:21]
	v_mfma_f32_16x16x32_bf16 v[6:9], v[164:167], v[212:215], v[6:9]
	v_mfma_f32_16x16x32_bf16 v[2:5], v[172:175], v[212:215], v[2:5]
	s_setprio 0
	s_barrier
	s_add_i32 s9, 0, 0x18000
	s_add_i32 s71, 0, 0x1c000
	v_add_u32_e32 v156, s9, v145
	v_add_u32_e32 v172, s71, v145
	s_add_u32 s54, s54, 0x80000
	s_addc_u32 s55, s55, 0
	s_mov_b32 m0, s64
	v_lshl_add_u64 v[236:237], s[54:55], 0, v[130:131]
	global_load_lds_dwordx4 v[236:237], off
	v_lshl_add_u64 v[236:237], s[54:55], 0, v[132:133]
	s_mov_b32 m0, s65
	s_nop 0
	global_load_lds_dwordx4 v[236:237], off
	ds_read_b128 v[140:143], v156
	ds_read_b128 v[148:151], v156 offset:1024
	ds_read_b128 v[152:155], v156 offset:2048
	ds_read_b128 v[156:159], v156 offset:3072
	ds_read_b128 v[160:163], v172
	ds_read_b128 v[164:167], v172 offset:1024
	ds_read_b128 v[168:171], v172 offset:2048
	ds_read_b128 v[172:175], v172 offset:3072
	ds_read_b128 v[176:179], v147 offset:32768
	ds_read_b128 v[180:183], v147 offset:33792
	ds_read_b128 v[184:187], v147 offset:34816
	ds_read_b128 v[188:191], v147 offset:35840
	ds_read_b128 v[200:203], v147 offset:36864
	ds_read_b128 v[204:207], v147 offset:37888
	ds_read_b128 v[208:211], v147 offset:38912
	ds_read_b128 v[212:215], v147 offset:39936
	s_waitcnt vmcnt(8)
	s_waitcnt lgkmcnt(0)
	s_barrier
	s_setprio 1
	s_waitcnt lgkmcnt(0)
	v_mfma_f32_16x16x32_bf16 v[126:129], v[140:143], v[176:179], v[126:129]
	v_mfma_f32_16x16x32_bf16 v[122:125], v[152:155], v[176:179], v[122:125]
	v_mfma_f32_16x16x32_bf16 v[110:113], v[140:143], v[184:187], v[110:113]
	v_mfma_f32_16x16x32_bf16 v[106:109], v[152:155], v[184:187], v[106:109]
	v_mfma_f32_16x16x32_bf16 v[94:97], v[140:143], v[200:203], v[94:97]
	v_mfma_f32_16x16x32_bf16 v[90:93], v[152:155], v[200:203], v[90:93]
	v_mfma_f32_16x16x32_bf16 v[78:81], v[140:143], v[208:211], v[78:81]
	v_mfma_f32_16x16x32_bf16 v[74:77], v[152:155], v[208:211], v[74:77]
	v_mfma_f32_16x16x32_bf16 v[126:129], v[148:151], v[180:183], v[126:129]
	v_mfma_f32_16x16x32_bf16 v[122:125], v[156:159], v[180:183], v[122:125]
	v_mfma_f32_16x16x32_bf16 v[110:113], v[148:151], v[188:191], v[110:113]
	v_mfma_f32_16x16x32_bf16 v[106:109], v[156:159], v[188:191], v[106:109]
	v_mfma_f32_16x16x32_bf16 v[94:97], v[148:151], v[204:207], v[94:97]
	v_mfma_f32_16x16x32_bf16 v[90:93], v[156:159], v[204:207], v[90:93]
	v_mfma_f32_16x16x32_bf16 v[78:81], v[148:151], v[212:215], v[78:81]
	v_mfma_f32_16x16x32_bf16 v[74:77], v[156:159], v[212:215], v[74:77]
	s_setprio 0
	s_setprio 1
	v_mfma_f32_16x16x32_bf16 v[118:121], v[160:163], v[176:179], v[118:121]
	v_mfma_f32_16x16x32_bf16 v[114:117], v[168:171], v[176:179], v[114:117]
	v_mfma_f32_16x16x32_bf16 v[102:105], v[160:163], v[184:187], v[102:105]
	v_mfma_f32_16x16x32_bf16 v[98:101], v[168:171], v[184:187], v[98:101]
	v_mfma_f32_16x16x32_bf16 v[86:89], v[160:163], v[200:203], v[86:89]
	v_mfma_f32_16x16x32_bf16 v[82:85], v[168:171], v[200:203], v[82:85]
	v_mfma_f32_16x16x32_bf16 v[70:73], v[160:163], v[208:211], v[70:73]
	v_mfma_f32_16x16x32_bf16 v[66:69], v[168:171], v[208:211], v[66:69]
	v_mfma_f32_16x16x32_bf16 v[118:121], v[164:167], v[180:183], v[118:121]
	v_mfma_f32_16x16x32_bf16 v[114:117], v[172:175], v[180:183], v[114:117]
	v_mfma_f32_16x16x32_bf16 v[102:105], v[164:167], v[188:191], v[102:105]
	v_mfma_f32_16x16x32_bf16 v[98:101], v[172:175], v[188:191], v[98:101]
	v_mfma_f32_16x16x32_bf16 v[86:89], v[164:167], v[204:207], v[86:89]
	v_mfma_f32_16x16x32_bf16 v[82:85], v[172:175], v[204:207], v[82:85]
	v_mfma_f32_16x16x32_bf16 v[70:73], v[164:167], v[212:215], v[70:73]
	v_mfma_f32_16x16x32_bf16 v[66:69], v[172:175], v[212:215], v[66:69]
	s_setprio 0
	s_barrier
; #define PG8_STAGE_A(bufoff, kptr, h) do { if constexpr (GATHER) { PG8_STAGE(bufoff, kptr, oa[h]); } else { PG8_STAGE(bufoff, (kptr) + (h) * hstep, voffA); } } while (0)
; #define PG8_STAGE(bufoff, gbase, voff) do { _Pragma("unroll") for (int _i = 0; _i < 2; ++_i) \
;         __builtin_amdgcn_global_load_lds((const unsigned*)((const char*)(gbase) + (voff)[_i]), (LAS unsigned*)(lds + (bufoff) + ldsw + _i * 8192), 16, 0, 0); } while (0)
; #define PG8_LDA(dst, b, h) do { _Pragma("unroll") for (int m = 0; m < 4; ++m) _Pragma("unroll") for (int k = 0; k < 2; ++k) dst[m][k] = *(const LAS bf16x8*)(lds + PG8_SA(b, h) + aoff + m * 2048 + k * 1024); } while (0)
; #define PG8_MMA(ai, bj, At, Bt) do { __builtin_amdgcn_s_setprio(1); _Pragma("unroll") for (int m = 0; m < 4; ++m) _Pragma("unroll") for (int n = 0; n < 2; ++n) _Pragma("unroll") for (int k = 0; k < 2; ++k) \
;         acc[ai][bj][m][n] = __builtin_amdgcn_mfma_f32_16x16x32_bf16(Bt[n][k], At[m][k], acc[ai][bj][m][n], 0, 0, 0); __builtin_amdgcn_s_setprio(0); } while (0)
; #define PG8_WAIT_V(n) asm volatile("s_waitcnt vmcnt(" #n ")" ::: "memory")
; #define PG8_WAIT_L(n) asm volatile("s_waitcnt lgkmcnt(" #n ")" ::: "memory")
; #define PG8_BAR __builtin_amdgcn_s_barrier()
; #define PG8_SCHED __builtin_amdgcn_sched_barrier(0)
; template <class Epi, class Sched, bool GATHER, bool SEGHOOK = false>
; __device__ __forceinline__ void gemm_phase(LAS unsigned char* lds, const int K, const Sched& S, const Epi& E, int tid_) {
;     ...
;             PG8_LDA(At, 1, 1); PG8_STAGE(PG8_SB(1, 0), b3, voffB); PG8_STAGE(PG8_SB(1, 1), b3 + hstep, voffB); PG8_STAGE_A(PG8_SA(1, 0), a3, 0);
;             PG8_WAIT_V(8); PG8_WAIT_L(0); PG8_BAR; PG8_MMA(1, 0, At, B0); PG8_MMA(1, 1, At, B1); PG8_BAR; PG8_SCHED;
;         }
	s_add_i32 s9, s9, s62
	v_lshl_add_u64 v[192:193], v[192:193], 0, s[90:91]
	s_mov_b32 m0, s9
	s_nop 0
	global_load_lds_dwordx4 v[192:193], off
	s_add_i32 m0, s9, 0x2000
	s_add_u32 s52, s52, 0x80080
	v_lshl_add_u64 v[192:193], v[216:217], 0, s[90:91]
	s_addc_u32 s53, s53, 0
	s_add_i32 s9, s71, s62
	global_load_lds_dwordx4 v[192:193], off
	v_lshl_add_u64 v[192:193], s[52:53], 0, v[0:1]
	s_mov_b32 m0, s9
	s_nop 0
	global_load_lds_dwordx4 v[192:193], off
	v_lshl_add_u64 v[192:193], s[52:53], 0, v[134:135]
	s_add_i32 m0, s9, 0x2000
	s_nop 0
	global_load_lds_dwordx4 v[192:193], off
	v_lshl_add_u64 v[192:193], v[218:219], 0, s[90:91]
	s_mov_b32 m0, s66
	s_nop 0
	global_load_lds_dwordx4 v[192:193], off
	v_lshl_add_u64 v[192:193], v[220:221], 0, s[90:91]
	s_mov_b32 m0, s67
	s_nop 0
	global_load_lds_dwordx4 v[192:193], off
	ds_read_b128 v[176:179], v147 offset:49152
	ds_read_b128 v[180:183], v147 offset:50176
	ds_read_b128 v[184:187], v147 offset:51200
	ds_read_b128 v[188:191], v147 offset:52224
	ds_read_b128 v[200:203], v147 offset:53248
	ds_read_b128 v[204:207], v147 offset:54272
	ds_read_b128 v[208:211], v147 offset:55296
	ds_read_b128 v[212:215], v147 offset:56320
	s_waitcnt vmcnt(8)
	s_waitcnt lgkmcnt(0)
	s_barrier
	s_setprio 1
	s_waitcnt lgkmcnt(0)
	v_mfma_f32_16x16x32_bf16 v[62:65], v[140:143], v[176:179], v[62:65]
	v_mfma_f32_16x16x32_bf16 v[58:61], v[152:155], v[176:179], v[58:61]
	v_mfma_f32_16x16x32_bf16 v[46:49], v[140:143], v[184:187], v[46:49]
	v_mfma_f32_16x16x32_bf16 v[42:45], v[152:155], v[184:187], v[42:45]
	v_mfma_f32_16x16x32_bf16 v[30:33], v[140:143], v[200:203], v[30:33]
	v_mfma_f32_16x16x32_bf16 v[26:29], v[152:155], v[200:203], v[26:29]
	v_mfma_f32_16x16x32_bf16 v[14:17], v[140:143], v[208:211], v[14:17]
	v_mfma_f32_16x16x32_bf16 v[10:13], v[152:155], v[208:211], v[10:13]
	v_mfma_f32_16x16x32_bf16 v[62:65], v[148:151], v[180:183], v[62:65]
	v_mfma_f32_16x16x32_bf16 v[58:61], v[156:159], v[180:183], v[58:61]
	v_mfma_f32_16x16x32_bf16 v[46:49], v[148:151], v[188:191], v[46:49]
	v_mfma_f32_16x16x32_bf16 v[42:45], v[156:159], v[188:191], v[42:45]
	v_mfma_f32_16x16x32_bf16 v[30:33], v[148:151], v[204:207], v[30:33]
	v_mfma_f32_16x16x32_bf16 v[26:29], v[156:159], v[204:207], v[26:29]
	v_mfma_f32_16x16x32_bf16 v[14:17], v[148:151], v[212:215], v[14:17]
	v_mfma_f32_16x16x32_bf16 v[10:13], v[156:159], v[212:215], v[10:13]
	s_setprio 0
	s_setprio 1
	v_mfma_f32_16x16x32_bf16 v[54:57], v[160:163], v[176:179], v[54:57]
	v_mfma_f32_16x16x32_bf16 v[50:53], v[168:171], v[176:179], v[50:53]
	v_mfma_f32_16x16x32_bf16 v[38:41], v[160:163], v[184:187], v[38:41]
	v_mfma_f32_16x16x32_bf16 v[34:37], v[168:171], v[184:187], v[34:37]
	v_mfma_f32_16x16x32_bf16 v[22:25], v[160:163], v[200:203], v[22:25]
	v_mfma_f32_16x16x32_bf16 v[18:21], v[168:171], v[200:203], v[18:21]
	v_mfma_f32_16x16x32_bf16 v[6:9], v[160:163], v[208:211], v[6:9]
	v_mfma_f32_16x16x32_bf16 v[2:5], v[168:171], v[208:211], v[2:5]
	v_mfma_f32_16x16x32_bf16 v[54:57], v[164:167], v[180:183], v[54:57]
	v_mfma_f32_16x16x32_bf16 v[50:53], v[172:175], v[180:183], v[50:53]
	v_mfma_f32_16x16x32_bf16 v[38:41], v[164:167], v[188:191], v[38:41]
	v_mfma_f32_16x16x32_bf16 v[34:37], v[172:175], v[188:191], v[34:37]
	v_mfma_f32_16x16x32_bf16 v[22:25], v[164:167], v[204:207], v[22:25]
	v_mfma_f32_16x16x32_bf16 v[18:21], v[172:175], v[204:207], v[18:21]
	v_mfma_f32_16x16x32_bf16 v[6:9], v[164:167], v[212:215], v[6:9]
	v_mfma_f32_16x16x32_bf16 v[2:5], v[172:175], v[212:215], v[2:5]
	s_setprio 0
	s_barrier
	s_add_i32 s70, s70, 2
	s_add_u32 s41, s41, 0x100
	s_addc_u32 s69, s69, 0
	s_add_u32 s50, s50, 0x100
	s_addc_u32 s51, s51, 0
	s_cmp_gt_u32 s70, 29
	s_cbranch_scc0 .LBB0_219
	s_and_b64 vcc, exec, s[10:11]
	s_cbranch_vccz .LBB0_222
	s_barrier
